# baseline (speedup 1.0000x reference)
.LBB3_6:
	s_or_b64 exec, exec, s[4:5]
	s_waitcnt vmcnt(4)
	v_cvt_f32_ubyte1_e32 v27, v14
	v_cvt_f32_ubyte0_e32 v26, v14
	v_cvt_f32_ubyte3_e32 v53, v14
	v_cvt_f32_ubyte2_e32 v52, v14
	v_cvt_f32_ubyte1_e32 v75, v15
	v_cvt_f32_ubyte0_e32 v74, v15
	v_cvt_f32_ubyte3_e32 v73, v15
	v_cvt_f32_ubyte2_e32 v72, v15
	v_cvt_f32_ubyte1_e32 v15, v16
	v_cvt_f32_ubyte0_e32 v14, v16
	v_cvt_f32_ubyte3_e32 v71, v16
	v_cvt_f32_ubyte2_e32 v70, v16
	v_cmp_lt_u32_e64 s[0:1], v94, v5
	v_add_u32_e32 v88, -1, v88
	v_cvt_f32_ubyte1_e32 v67, v17
	v_cvt_f32_ubyte0_e32 v66, v17
	v_cvt_f32_ubyte3_e32 v65, v17
	v_cvt_f32_ubyte2_e32 v64, v17
	v_fmac_f32_e32 v68, v70, v48
	v_fmac_f32_e32 v69, v71, v48
	v_fma_f32 v70, v14, v48, v62
	v_fma_f32 v71, v15, v48, v63
	v_cndmask_b32_e64 v14, v51, v97, s[0:1]
	v_cmp_eq_u32_e64 s[0:1], 0, v88
	v_fma_f32 v64, v64, v48, v24
	v_fma_f32 v65, v65, v48, v25
	v_fma_f32 v66, v66, v48, v36
	v_fma_f32 v67, v67, v48, v37
	v_fma_f32 v72, v72, v48, v22
	v_fma_f32 v73, v73, v48, v23
	v_fma_f32 v74, v74, v48, v58
	v_fma_f32 v75, v75, v48, v59
	v_fma_f32 v76, v52, v48, v34
	v_fma_f32 v77, v53, v48, v35
	v_fma_f32 v78, v26, v48, v28
	v_fma_f32 v79, v27, v48, v29
	v_add_u32_e32 v94, 8, v94
	s_or_b64 s[16:17], s[0:1], s[16:17]
	v_mov_b32_e32 v95, v96
	v_mov_b32_e32 v96, v14
	s_andn2_b64 exec, exec, s[16:17]
	s_cbranch_execz .LBB3_23

.LBB3_9:
	s_or_b64 exec, exec, s[4:5]
	s_waitcnt vmcnt(5)
	v_cvt_f32_ubyte1_e32 v101, v30
	v_cvt_f32_ubyte0_e32 v100, v30
	v_fmac_f32_e32 v78, v100, v56
	v_fmac_f32_e32 v79, v101, v56
	v_cvt_f32_ubyte3_e32 v101, v30
	v_cvt_f32_ubyte2_e32 v100, v30
	v_fmac_f32_e32 v76, v100, v56
	v_fmac_f32_e32 v77, v101, v56
	v_cvt_f32_ubyte1_e32 v101, v31
	v_cvt_f32_ubyte0_e32 v100, v31
	v_fmac_f32_e32 v74, v100, v56
	v_fmac_f32_e32 v75, v101, v56
	v_cvt_f32_ubyte3_e32 v101, v31
	v_cvt_f32_ubyte2_e32 v100, v31
	v_cvt_f32_ubyte1_e32 v31, v32
	v_cvt_f32_ubyte0_e32 v30, v32
	v_fmac_f32_e32 v70, v30, v56
	v_fmac_f32_e32 v71, v31, v56
	v_cvt_f32_ubyte3_e32 v31, v32
	v_cvt_f32_ubyte2_e32 v30, v32
	v_fmac_f32_e32 v68, v30, v56
	v_fmac_f32_e32 v69, v31, v56
	v_cvt_f32_ubyte1_e32 v31, v33
	v_cvt_f32_ubyte0_e32 v30, v33
	v_fmac_f32_e32 v66, v30, v56
	v_fmac_f32_e32 v67, v31, v56
	v_cvt_f32_ubyte3_e32 v31, v33
	v_cvt_f32_ubyte2_e32 v30, v33
	v_and_b32_e32 v32, 2, v52
	v_fmac_f32_e32 v72, v100, v56
	v_fmac_f32_e32 v73, v101, v56
	v_fma_f32 v30, v30, v56, v64
	v_fma_f32 v31, v31, v56, v65
	v_cmp_ne_u32_e64 s[0:1], 0, v32
	s_and_saveexec_b64 s[4:5], s[0:1]
	s_cbranch_execz .LBB3_11
	v_and_b32_e32 v32, 63, v98
	v_mul_u32_u24_e32 v32, 0x220, v32
	v_or_b32_e32 v42, v49, v32
	ds_read2_b32 v[32:33], v42 offset1:8
	ds_read2_b32 v[64:65], v42 offset0:16 offset1:24
	ds_read2_b32 v[98:99], v42 offset0:32 offset1:40
	ds_bpermute_b32 v63, v85, v95
	s_waitcnt lgkmcnt(3)
	v_add_f32_e32 v32, v78, v32
	v_add_f32_e32 v33, v79, v33
	s_waitcnt lgkmcnt(2)
	v_add_f32_e32 v53, v76, v64
	ds_write2_b32 v42, v32, v33 offset1:8
	v_add_f32_e32 v32, v77, v65
	ds_write2_b32 v42, v53, v32 offset0:16 offset1:24
	ds_read2_b32 v[32:33], v42 offset0:48 offset1:56
	ds_read2_b32 v[64:65], v42 offset0:64 offset1:72
	s_waitcnt lgkmcnt(5)
	v_add_f32_e32 v53, v74, v98
	v_add_f32_e32 v59, v75, v99
	ds_write2_b32 v42, v53, v59 offset0:32 offset1:40
	s_waitcnt lgkmcnt(2)
	v_add_f32_e32 v32, v72, v32
	v_add_f32_e32 v33, v73, v33
	ds_write2_b32 v42, v32, v33 offset0:48 offset1:56
	ds_read2_b32 v[32:33], v42 offset0:80 offset1:88
	s_waitcnt lgkmcnt(3)
	v_add_f32_e32 v53, v70, v64
	v_add_f32_e32 v59, v71, v65
	ds_read2_b32 v[64:65], v42 offset0:96 offset1:104
	ds_write2_b32 v42, v53, v59 offset0:64 offset1:72
	s_waitcnt lgkmcnt(2)
	v_add_f32_e32 v32, v68, v32
	v_add_f32_e32 v33, v69, v33
	ds_write2_b32 v42, v32, v33 offset0:80 offset1:88
	ds_read2_b32 v[32:33], v42 offset0:112 offset1:120
	s_waitcnt lgkmcnt(3)
	v_add_f32_e32 v53, v66, v64
	v_add_f32_e32 v59, v67, v65
	v_lshrrev_b32_e32 v98, 16, v63
	ds_write2_b32 v42, v53, v59 offset0:96 offset1:104
	s_waitcnt lgkmcnt(1)
	v_add_f32_e32 v30, v30, v32
	v_add_f32_e32 v31, v31, v33
	ds_write2_b32 v42, v30, v31 offset0:112 offset1:120
	v_mov_b32_e32 v30, 0
	v_mov_b32_e32 v31, v30
	v_mov_b32_e32 v66, v30
	v_mov_b32_e32 v67, v30
	v_mov_b32_e32 v68, v30
	v_mov_b32_e32 v69, v30
	v_mov_b32_e32 v70, v30
	v_mov_b32_e32 v71, v30
	v_mov_b32_e32 v72, v30
	v_mov_b32_e32 v73, v30
	v_mov_b32_e32 v74, v30
	v_mov_b32_e32 v75, v30
	v_mov_b32_e32 v76, v30
	v_mov_b32_e32 v77, v30
	v_mov_b32_e32 v78, v30
	v_mov_b32_e32 v79, v30
.LBB3_11:
	s_or_b64 exec, exec, s[4:5]
	v_cvt_f32_ubyte1_e32 v33, v18
	v_cvt_f32_ubyte0_e32 v32, v18
	v_fmac_f32_e32 v78, v32, v57
	v_fmac_f32_e32 v79, v33, v57
	v_cvt_f32_ubyte3_e32 v33, v18
	v_cvt_f32_ubyte2_e32 v32, v18
	v_fmac_f32_e32 v76, v32, v57
	v_fmac_f32_e32 v77, v33, v57
	v_cvt_f32_ubyte1_e32 v33, v19
	v_cvt_f32_ubyte0_e32 v32, v19
	v_fmac_f32_e32 v74, v32, v57
	v_fmac_f32_e32 v75, v33, v57
	v_cvt_f32_ubyte3_e32 v33, v19
	v_cvt_f32_ubyte2_e32 v32, v19
	v_cvt_f32_ubyte1_e32 v19, v20
	v_cvt_f32_ubyte0_e32 v18, v20
	v_fmac_f32_e32 v70, v18, v57
	v_fmac_f32_e32 v71, v19, v57
	v_cvt_f32_ubyte3_e32 v19, v20
	v_cvt_f32_ubyte2_e32 v18, v20
	v_fma_f32 v64, v18, v57, v68
	v_fma_f32 v65, v19, v57, v69
	v_cvt_f32_ubyte1_e32 v19, v21
	v_cvt_f32_ubyte0_e32 v18, v21
	v_fmac_f32_e32 v72, v32, v57
	v_fmac_f32_e32 v73, v33, v57
	v_fma_f32 v32, v18, v57, v66
	v_fma_f32 v33, v19, v57, v67
	v_cvt_f32_ubyte3_e32 v19, v21
	v_cvt_f32_ubyte2_e32 v18, v21
	v_and_b32_e32 v20, 4, v52
	v_fma_f32 v18, v18, v57, v30
	v_fma_f32 v19, v19, v57, v31
	v_cmp_ne_u32_e64 s[0:1], 0, v20
	s_and_saveexec_b64 s[4:5], s[0:1]
	s_cbranch_execz .LBB3_13
	v_and_b32_e32 v20, 63, v98
	v_mul_u32_u24_e32 v20, 0x220, v20
	v_or_b32_e32 v42, v49, v20
	ds_read2_b32 v[20:21], v42 offset1:8
	ds_read2_b32 v[30:31], v42 offset0:16 offset1:24
	ds_read2_b32 v[56:57], v42 offset0:32 offset1:40
	s_waitcnt lgkmcnt(2)
	v_add_f32_e32 v20, v78, v20
	v_add_f32_e32 v21, v79, v21
	s_waitcnt lgkmcnt(1)
	v_add_f32_e32 v30, v76, v30
	ds_write2_b32 v42, v20, v21 offset1:8
	v_add_f32_e32 v20, v77, v31
	ds_write2_b32 v42, v30, v20 offset0:16 offset1:24
	ds_read2_b32 v[20:21], v42 offset0:48 offset1:56
	s_waitcnt lgkmcnt(3)
	v_add_f32_e32 v30, v74, v56
	v_add_f32_e32 v31, v75, v57
	ds_write2_b32 v42, v30, v31 offset0:32 offset1:40
	ds_read2_b32 v[30:31], v42 offset0:64 offset1:72
	s_waitcnt lgkmcnt(2)
	v_add_f32_e32 v20, v72, v20
	v_add_f32_e32 v21, v73, v21
	ds_write2_b32 v42, v20, v21 offset0:48 offset1:56
	ds_read2_b32 v[20:21], v42 offset0:80 offset1:88
	s_waitcnt lgkmcnt(2)
	v_add_f32_e32 v30, v70, v30
	v_add_f32_e32 v31, v71, v31
	ds_write2_b32 v42, v30, v31 offset0:64 offset1:72
	ds_read2_b32 v[30:31], v42 offset0:96 offset1:104
	s_waitcnt lgkmcnt(2)
	v_add_f32_e32 v20, v64, v20
	v_add_f32_e32 v21, v65, v21
	ds_write2_b32 v42, v20, v21 offset0:80 offset1:88
	ds_read2_b32 v[20:21], v42 offset0:112 offset1:120
	s_waitcnt lgkmcnt(2)
	v_add_f32_e32 v30, v32, v30
	ds_bpermute_b32 v32, v86, v95
	v_add_f32_e32 v31, v33, v31
	ds_write2_b32 v42, v30, v31 offset0:96 offset1:104
	s_waitcnt lgkmcnt(2)
	v_add_f32_e32 v18, v18, v20
	v_add_f32_e32 v19, v19, v21
	ds_write2_b32 v42, v18, v19 offset0:112 offset1:120
	v_mov_b32_e32 v18, 0
	s_waitcnt lgkmcnt(2)
	v_lshrrev_b32_e32 v98, 16, v32
	v_mov_b32_e32 v19, v18
	v_mov_b32_e32 v32, v18
	v_mov_b32_e32 v33, v18
	v_mov_b32_e32 v64, v18
	v_mov_b32_e32 v65, v18
	v_mov_b32_e32 v70, v18
	v_mov_b32_e32 v71, v18
	v_mov_b32_e32 v72, v18
	v_mov_b32_e32 v73, v18
	v_mov_b32_e32 v74, v18
	v_mov_b32_e32 v75, v18
	v_mov_b32_e32 v76, v18
	v_mov_b32_e32 v77, v18
	v_mov_b32_e32 v78, v18
	v_mov_b32_e32 v79, v18
.LBB3_13:
	s_or_b64 exec, exec, s[4:5]
	v_cvt_f32_ubyte1_e32 v21, v10
	v_cvt_f32_ubyte0_e32 v20, v10
	v_fmac_f32_e32 v78, v20, v50
	v_fmac_f32_e32 v79, v21, v50
	v_cvt_f32_ubyte3_e32 v21, v10
	v_cvt_f32_ubyte2_e32 v20, v10
	v_fmac_f32_e32 v76, v20, v50
	v_fmac_f32_e32 v77, v21, v50
	v_cvt_f32_ubyte1_e32 v21, v11
	v_cvt_f32_ubyte0_e32 v20, v11
	v_fma_f32 v68, v20, v50, v74
	v_fma_f32 v69, v21, v50, v75
	v_cvt_f32_ubyte3_e32 v21, v11
	v_cvt_f32_ubyte2_e32 v20, v11
	v_cvt_f32_ubyte1_e32 v11, v12
	v_cvt_f32_ubyte0_e32 v10, v12
	v_fma_f32 v56, v10, v50, v70
	v_fma_f32 v57, v11, v50, v71
	v_cvt_f32_ubyte3_e32 v11, v12
	v_cvt_f32_ubyte2_e32 v10, v12
	v_fma_f32 v30, v10, v50, v64
	v_fma_f32 v31, v11, v50, v65
	v_cvt_f32_ubyte1_e32 v11, v13
	v_cvt_f32_ubyte0_e32 v10, v13
	v_fma_f32 v66, v20, v50, v72
	v_fma_f32 v67, v21, v50, v73
	v_fma_f32 v20, v10, v50, v32
	v_fma_f32 v21, v11, v50, v33
	v_cvt_f32_ubyte3_e32 v11, v13
	v_cvt_f32_ubyte2_e32 v10, v13
	v_and_b32_e32 v12, 8, v52
	v_fma_f32 v10, v10, v50, v18
	v_fma_f32 v11, v11, v50, v19
	v_cmp_ne_u32_e64 s[0:1], 0, v12
	s_and_saveexec_b64 s[4:5], s[0:1]
	s_cbranch_execz .LBB3_15
	v_and_b32_e32 v12, 63, v98
	v_mul_u32_u24_e32 v12, 0x220, v12
	v_or_b32_e32 v42, v49, v12
	ds_read2_b32 v[12:13], v42 offset1:8
	ds_read2_b32 v[18:19], v42 offset0:16 offset1:24
	ds_read2_b32 v[32:33], v42 offset0:32 offset1:40
	s_waitcnt lgkmcnt(2)
	v_add_f32_e32 v12, v78, v12
	v_add_f32_e32 v13, v79, v13
	s_waitcnt lgkmcnt(1)
	v_add_f32_e32 v18, v76, v18
	ds_write2_b32 v42, v12, v13 offset1:8
	v_add_f32_e32 v12, v77, v19
	ds_write2_b32 v42, v18, v12 offset0:16 offset1:24
	ds_read2_b32 v[12:13], v42 offset0:48 offset1:56
	s_waitcnt lgkmcnt(3)
	v_add_f32_e32 v18, v68, v32
	v_add_f32_e32 v19, v69, v33
	ds_write2_b32 v42, v18, v19 offset0:32 offset1:40
	ds_read2_b32 v[18:19], v42 offset0:64 offset1:72
	s_waitcnt lgkmcnt(2)
	v_add_f32_e32 v12, v66, v12
	v_add_f32_e32 v13, v67, v13
	ds_write2_b32 v42, v12, v13 offset0:48 offset1:56
	ds_read2_b32 v[12:13], v42 offset0:80 offset1:88
	s_waitcnt lgkmcnt(2)
	v_add_f32_e32 v18, v56, v18
	v_add_f32_e32 v19, v57, v19
	ds_write2_b32 v42, v18, v19 offset0:64 offset1:72
	ds_read2_b32 v[18:19], v42 offset0:96 offset1:104
	s_waitcnt lgkmcnt(2)
	v_add_f32_e32 v12, v30, v12
	v_add_f32_e32 v13, v31, v13
	ds_write2_b32 v42, v12, v13 offset0:80 offset1:88
	ds_read2_b32 v[12:13], v42 offset0:112 offset1:120
	s_waitcnt lgkmcnt(2)
	v_add_f32_e32 v18, v20, v18
	ds_bpermute_b32 v20, v87, v95
	v_add_f32_e32 v19, v21, v19
	ds_write2_b32 v42, v18, v19 offset0:96 offset1:104
	s_waitcnt lgkmcnt(2)
	v_add_f32_e32 v10, v10, v12
	v_add_f32_e32 v11, v11, v13
	ds_write2_b32 v42, v10, v11 offset0:112 offset1:120
	v_mov_b32_e32 v10, 0
	s_waitcnt lgkmcnt(2)
	v_lshrrev_b32_e32 v98, 16, v20
	v_mov_b32_e32 v11, v10
	v_mov_b32_e32 v20, v10
	v_mov_b32_e32 v21, v10
	v_mov_b32_e32 v30, v10
	v_mov_b32_e32 v31, v10
	v_mov_b32_e32 v56, v10
	v_mov_b32_e32 v57, v10
	v_mov_b32_e32 v66, v10
	v_mov_b32_e32 v67, v10
	v_mov_b32_e32 v68, v10
	v_mov_b32_e32 v69, v10
	v_mov_b32_e32 v76, v10
	v_mov_b32_e32 v77, v10
	v_mov_b32_e32 v78, v10
	v_mov_b32_e32 v79, v10
.LBB3_15:
	s_or_b64 exec, exec, s[4:5]
	v_cvt_f32_ubyte1_e32 v13, v6
	v_cvt_f32_ubyte0_e32 v12, v6
	v_fmac_f32_e32 v78, v12, v46
	v_fmac_f32_e32 v79, v13, v46
	v_cvt_f32_ubyte3_e32 v13, v6
	v_cvt_f32_ubyte2_e32 v12, v6
	v_fmac_f32_e32 v76, v12, v46
	v_fmac_f32_e32 v77, v13, v46
	v_cvt_f32_ubyte1_e32 v13, v7
	v_cvt_f32_ubyte0_e32 v12, v7
	v_fma_f32 v74, v12, v46, v68
	v_fma_f32 v75, v13, v46, v69
	v_cvt_f32_ubyte3_e32 v13, v7
	v_cvt_f32_ubyte2_e32 v12, v7
	v_cvt_f32_ubyte1_e32 v7, v8
	v_cvt_f32_ubyte0_e32 v6, v8
	v_fma_f32 v70, v6, v46, v56
	v_fma_f32 v71, v7, v46, v57
	v_cvt_f32_ubyte3_e32 v7, v8
	v_cvt_f32_ubyte2_e32 v6, v8
	v_fma_f32 v68, v6, v46, v30
	v_fma_f32 v69, v7, v46, v31
	v_cvt_f32_ubyte1_e32 v7, v9
	v_cvt_f32_ubyte0_e32 v6, v9
	v_fma_f32 v72, v12, v46, v66
	v_fma_f32 v73, v13, v46, v67
	v_fma_f32 v66, v6, v46, v20
	v_fma_f32 v67, v7, v46, v21
	v_cvt_f32_ubyte3_e32 v7, v9
	v_cvt_f32_ubyte2_e32 v6, v9
	v_fma_f32 v64, v6, v46, v10
	v_fma_f32 v65, v7, v46, v11
	s_setprio 3
	ds_bpermute_b32 v6, v55, v96
	ds_bpermute_b32 v7, v85, v96
	ds_bpermute_b32 v8, v86, v96
	ds_bpermute_b32 v9, v87, v96
	s_waitcnt lgkmcnt(3)
	v_and_b32_e32 v46, 0xffff, v6
	s_waitcnt lgkmcnt(2)
	v_and_b32_e32 v50, 0xffff, v7
	v_lshlrev_b32_e32 v42, 7, v46
	v_lshl_add_u64 v[6:7], v[44:45], 0, v[42:43]
	v_lshlrev_b32_e32 v42, 7, v50
	s_waitcnt lgkmcnt(1)
	v_and_b32_e32 v53, 0xffff, v8
	global_load_dwordx4 v[30:33], v[6:7], off
	v_lshl_add_u64 v[6:7], v[44:45], 0, v[42:43]
	v_lshlrev_b32_e32 v42, 7, v53
	s_waitcnt lgkmcnt(0)
	v_and_b32_e32 v59, 0xffff, v9
	global_load_dwordx4 v[18:21], v[6:7], off
	v_lshl_add_u64 v[6:7], v[44:45], 0, v[42:43]
	v_lshlrev_b32_e32 v42, 7, v59
	global_load_dwordx4 v[10:13], v[6:7], off
	v_lshl_add_u64 v[6:7], v[44:45], 0, v[42:43]
	global_load_dwordx4 v[6:9], v[6:7], off
	v_mul_hi_u32 v42, v46, s19
	v_lshlrev_b32_e32 v42, 2, v42
	ds_read_b32 v56, v42 offset:34816
	v_mul_hi_u32 v42, v50, s19
	v_lshlrev_b32_e32 v42, 2, v42
	ds_read_b32 v57, v42 offset:34816
	v_mul_hi_u32 v42, v53, s19
	v_lshlrev_b32_e32 v42, 2, v42
	ds_read_b32 v50, v42 offset:34816
	v_mul_hi_u32 v42, v59, s19
	v_lshlrev_b32_e32 v42, 2, v42
	ds_read_b32 v46, v42 offset:34816
	s_setprio 1
	v_and_b32_e32 v42, 16, v52
	v_cmp_ne_u32_e64 s[0:1], 0, v42
	s_and_saveexec_b64 s[4:5], s[0:1]
	s_cbranch_execz .LBB3_17
	v_and_b32_e32 v42, 63, v98
	v_mul_u32_u24_e32 v42, 0x220, v42
	v_or_b32_e32 v42, v49, v42
	ds_read2_b32 v[98:99], v42 offset1:8
	ds_read2_b32 v[100:101], v42 offset0:16 offset1:24
	ds_read2_b32 v[102:103], v42 offset0:32 offset1:40
	s_waitcnt lgkmcnt(2)
	v_add_f32_e32 v53, v78, v98
	v_add_f32_e32 v59, v79, v99
	s_waitcnt lgkmcnt(1)
	v_add_f32_e32 v63, v76, v100
	ds_write2_b32 v42, v53, v59 offset1:8
	v_add_f32_e32 v53, v77, v101
	ds_read2_b32 v[76:77], v42 offset0:48 offset1:56
	ds_write2_b32 v42, v63, v53 offset0:16 offset1:24
	s_waitcnt lgkmcnt(3)
	v_add_f32_e32 v53, v74, v102
	v_add_f32_e32 v59, v75, v103
	ds_read2_b32 v[74:75], v42 offset0:64 offset1:72
	ds_write2_b32 v42, v53, v59 offset0:32 offset1:40
	s_waitcnt lgkmcnt(3)
	v_add_f32_e32 v53, v72, v76
	v_add_f32_e32 v59, v73, v77
	ds_read2_b32 v[72:73], v42 offset0:80 offset1:88
	ds_write2_b32 v42, v53, v59 offset0:48 offset1:56
	s_waitcnt lgkmcnt(3)
	v_add_f32_e32 v53, v70, v74
	v_add_f32_e32 v59, v71, v75
	ds_read2_b32 v[70:71], v42 offset0:96 offset1:104
	ds_write2_b32 v42, v53, v59 offset0:64 offset1:72
	s_waitcnt lgkmcnt(3)
	v_add_f32_e32 v53, v68, v72
	v_add_f32_e32 v59, v69, v73
	ds_read2_b32 v[68:69], v42 offset0:112 offset1:120
	ds_bpermute_b32 v63, v90, v95
	ds_write2_b32 v42, v53, v59 offset0:80 offset1:88
	s_waitcnt lgkmcnt(4)
	v_add_f32_e32 v53, v66, v70
	v_add_f32_e32 v59, v67, v71
	ds_write2_b32 v42, v53, v59 offset0:96 offset1:104
	s_waitcnt lgkmcnt(3)
	v_add_f32_e32 v53, v64, v68
	v_mov_b32_e32 v64, 0
	v_add_f32_e32 v59, v65, v69
	s_waitcnt lgkmcnt(2)
	v_lshrrev_b32_e32 v98, 16, v63
	v_mov_b32_e32 v65, v64
	v_mov_b32_e32 v78, v64
	v_mov_b32_e32 v79, v64
	v_mov_b32_e32 v76, v64
	v_mov_b32_e32 v77, v64
	v_mov_b32_e32 v74, v64
	v_mov_b32_e32 v75, v64
	v_mov_b32_e32 v72, v64
	v_mov_b32_e32 v73, v64
	v_mov_b32_e32 v70, v64
	v_mov_b32_e32 v71, v64
	v_mov_b32_e32 v68, v64
	v_mov_b32_e32 v69, v64
	v_mov_b32_e32 v66, v64
	v_mov_b32_e32 v67, v64
	ds_write2_b32 v42, v53, v59 offset0:112 offset1:120
.LBB3_17:
	s_or_b64 exec, exec, s[4:5]
	s_waitcnt vmcnt(7)
	v_cvt_f32_ubyte1_e32 v101, v34
	v_cvt_f32_ubyte0_e32 v100, v34
	v_fmac_f32_e32 v78, v100, v62
	v_fmac_f32_e32 v79, v101, v62
	v_cvt_f32_ubyte3_e32 v101, v34
	v_cvt_f32_ubyte2_e32 v100, v34
	v_fmac_f32_e32 v76, v100, v62
	v_fmac_f32_e32 v77, v101, v62
	v_cvt_f32_ubyte1_e32 v101, v35
	v_cvt_f32_ubyte0_e32 v100, v35
	v_fmac_f32_e32 v74, v100, v62
	v_fmac_f32_e32 v75, v101, v62
	v_cvt_f32_ubyte3_e32 v101, v35
	v_cvt_f32_ubyte2_e32 v100, v35
	v_cvt_f32_ubyte1_e32 v35, v36
	v_cvt_f32_ubyte0_e32 v34, v36
	v_fmac_f32_e32 v70, v34, v62
	v_fmac_f32_e32 v71, v35, v62
	v_cvt_f32_ubyte3_e32 v35, v36
	v_cvt_f32_ubyte2_e32 v34, v36
	v_fmac_f32_e32 v68, v34, v62
	v_fmac_f32_e32 v69, v35, v62
	v_cvt_f32_ubyte1_e32 v35, v37
	v_cvt_f32_ubyte0_e32 v34, v37
	v_fmac_f32_e32 v66, v34, v62
	v_fmac_f32_e32 v67, v35, v62
	v_cvt_f32_ubyte3_e32 v35, v37
	v_cvt_f32_ubyte2_e32 v34, v37
	v_and_b32_e32 v36, 32, v52
	v_fmac_f32_e32 v72, v100, v62
	v_fmac_f32_e32 v73, v101, v62
	v_fma_f32 v34, v34, v62, v64
	v_fma_f32 v35, v35, v62, v65
	v_cmp_ne_u32_e64 s[0:1], 0, v36
	s_and_saveexec_b64 s[4:5], s[0:1]
	s_cbranch_execz .LBB3_19
	v_and_b32_e32 v36, 63, v98
	v_mul_u32_u24_e32 v36, 0x220, v36
	v_or_b32_e32 v42, v49, v36
	ds_read2_b32 v[36:37], v42 offset1:8
	ds_read2_b32 v[62:63], v42 offset0:16 offset1:24
	ds_read2_b32 v[64:65], v42 offset0:32 offset1:40
	s_waitcnt lgkmcnt(2)
	v_add_f32_e32 v36, v78, v36
	v_add_f32_e32 v37, v79, v37
	s_waitcnt lgkmcnt(1)
	v_add_f32_e32 v53, v76, v62
	ds_write2_b32 v42, v36, v37 offset1:8
	v_add_f32_e32 v36, v77, v63
	ds_write2_b32 v42, v53, v36 offset0:16 offset1:24
	ds_read2_b32 v[36:37], v42 offset0:48 offset1:56
	ds_read2_b32 v[62:63], v42 offset0:64 offset1:72
	s_waitcnt lgkmcnt(4)
	v_add_f32_e32 v53, v74, v64
	v_add_f32_e32 v59, v75, v65
	ds_write2_b32 v42, v53, v59 offset0:32 offset1:40
	s_waitcnt lgkmcnt(2)
	v_add_f32_e32 v36, v72, v36
	v_add_f32_e32 v37, v73, v37
	ds_write2_b32 v42, v36, v37 offset0:48 offset1:56
	ds_read2_b32 v[36:37], v42 offset0:80 offset1:88
	s_waitcnt lgkmcnt(3)
	v_add_f32_e32 v53, v70, v62
	v_add_f32_e32 v59, v71, v63
	ds_read2_b32 v[62:63], v42 offset0:96 offset1:104
	ds_write2_b32 v42, v53, v59 offset0:64 offset1:72
	s_waitcnt lgkmcnt(2)
	v_add_f32_e32 v36, v68, v36
	v_add_f32_e32 v37, v69, v37
	ds_write2_b32 v42, v36, v37 offset0:80 offset1:88
	ds_read2_b32 v[36:37], v42 offset0:112 offset1:120
	s_waitcnt lgkmcnt(3)
	v_add_f32_e32 v53, v66, v62
	ds_bpermute_b32 v62, v91, v95
	v_add_f32_e32 v59, v67, v63
	ds_write2_b32 v42, v53, v59 offset0:96 offset1:104
	s_waitcnt lgkmcnt(2)
	v_add_f32_e32 v34, v34, v36
	v_add_f32_e32 v35, v35, v37
	ds_write2_b32 v42, v34, v35 offset0:112 offset1:120
	v_mov_b32_e32 v34, 0
	s_waitcnt lgkmcnt(2)
	v_lshrrev_b32_e32 v98, 16, v62
	v_mov_b32_e32 v35, v34
	v_mov_b32_e32 v66, v34
	v_mov_b32_e32 v67, v34
	v_mov_b32_e32 v68, v34
	v_mov_b32_e32 v69, v34
	v_mov_b32_e32 v70, v34
	v_mov_b32_e32 v71, v34
	v_mov_b32_e32 v72, v34
	v_mov_b32_e32 v73, v34
	v_mov_b32_e32 v74, v34
	v_mov_b32_e32 v75, v34
	v_mov_b32_e32 v76, v34
	v_mov_b32_e32 v77, v34
	v_mov_b32_e32 v78, v34
	v_mov_b32_e32 v79, v34
.LBB3_19:
	s_or_b64 exec, exec, s[4:5]
	s_waitcnt vmcnt(6)
	v_cvt_f32_ubyte1_e32 v37, v26
	v_cvt_f32_ubyte0_e32 v36, v26
	v_fmac_f32_e32 v78, v36, v58
	v_fmac_f32_e32 v79, v37, v58
	v_cvt_f32_ubyte3_e32 v37, v26
	v_cvt_f32_ubyte2_e32 v36, v26
	v_fmac_f32_e32 v76, v36, v58
	v_fmac_f32_e32 v77, v37, v58
	v_cvt_f32_ubyte1_e32 v37, v27
	v_cvt_f32_ubyte0_e32 v36, v27
	v_fmac_f32_e32 v74, v36, v58
	v_fmac_f32_e32 v75, v37, v58
	v_cvt_f32_ubyte3_e32 v37, v27
	v_cvt_f32_ubyte2_e32 v36, v27
	v_cvt_f32_ubyte1_e32 v27, v28
	v_cvt_f32_ubyte0_e32 v26, v28
	v_fma_f32 v62, v26, v58, v70
	v_fma_f32 v63, v27, v58, v71
	v_cvt_f32_ubyte3_e32 v27, v28
	v_cvt_f32_ubyte2_e32 v26, v28
	v_fma_f32 v64, v26, v58, v68
	v_fma_f32 v65, v27, v58, v69
	v_cvt_f32_ubyte1_e32 v27, v29
	v_cvt_f32_ubyte0_e32 v26, v29
	v_fmac_f32_e32 v72, v36, v58
	v_fmac_f32_e32 v73, v37, v58
	v_fma_f32 v36, v26, v58, v66
	v_fma_f32 v37, v27, v58, v67
	v_cvt_f32_ubyte3_e32 v27, v29
	v_cvt_f32_ubyte2_e32 v26, v29
	v_and_b32_e32 v28, 64, v52
	v_fma_f32 v26, v26, v58, v34
	v_fma_f32 v27, v27, v58, v35
	v_cmp_ne_u32_e64 s[0:1], 0, v28
	s_and_saveexec_b64 s[4:5], s[0:1]
	s_cbranch_execz .LBB3_21
	v_and_b32_e32 v28, 63, v98
	v_mul_u32_u24_e32 v28, 0x220, v28
	v_or_b32_e32 v42, v49, v28
	ds_read2_b32 v[28:29], v42 offset1:8
	ds_read2_b32 v[34:35], v42 offset0:16 offset1:24
	ds_read2_b32 v[58:59], v42 offset0:32 offset1:40
	s_waitcnt lgkmcnt(2)
	v_add_f32_e32 v28, v78, v28
	v_add_f32_e32 v29, v79, v29
	s_waitcnt lgkmcnt(1)
	v_add_f32_e32 v34, v76, v34
	ds_write2_b32 v42, v28, v29 offset1:8
	v_add_f32_e32 v28, v77, v35
	ds_write2_b32 v42, v34, v28 offset0:16 offset1:24
	ds_read2_b32 v[28:29], v42 offset0:48 offset1:56
	s_waitcnt lgkmcnt(3)
	v_add_f32_e32 v34, v74, v58
	v_add_f32_e32 v35, v75, v59
	ds_write2_b32 v42, v34, v35 offset0:32 offset1:40
	ds_read2_b32 v[34:35], v42 offset0:64 offset1:72
	s_waitcnt lgkmcnt(2)
	v_add_f32_e32 v28, v72, v28
	v_add_f32_e32 v29, v73, v29
	ds_write2_b32 v42, v28, v29 offset0:48 offset1:56
	ds_read2_b32 v[28:29], v42 offset0:80 offset1:88
	s_waitcnt lgkmcnt(2)
	v_add_f32_e32 v34, v62, v34
	v_add_f32_e32 v35, v63, v35
	ds_write2_b32 v42, v34, v35 offset0:64 offset1:72
	ds_read2_b32 v[34:35], v42 offset0:96 offset1:104
	s_waitcnt lgkmcnt(2)
	v_add_f32_e32 v28, v64, v28
	v_add_f32_e32 v29, v65, v29
	ds_write2_b32 v42, v28, v29 offset0:80 offset1:88
	ds_read2_b32 v[28:29], v42 offset0:112 offset1:120
	s_waitcnt lgkmcnt(2)
	v_add_f32_e32 v34, v36, v34
	ds_bpermute_b32 v36, v92, v95
	v_add_f32_e32 v35, v37, v35
	ds_write2_b32 v42, v34, v35 offset0:96 offset1:104
	s_waitcnt lgkmcnt(2)
	v_add_f32_e32 v26, v26, v28
	v_add_f32_e32 v27, v27, v29
	ds_write2_b32 v42, v26, v27 offset0:112 offset1:120
	v_mov_b32_e32 v26, 0
	s_waitcnt lgkmcnt(2)
	v_lshrrev_b32_e32 v98, 16, v36
	v_mov_b32_e32 v27, v26
	v_mov_b32_e32 v36, v26
	v_mov_b32_e32 v37, v26
	v_mov_b32_e32 v64, v26
	v_mov_b32_e32 v65, v26
	v_mov_b32_e32 v62, v26
	v_mov_b32_e32 v63, v26
	v_mov_b32_e32 v72, v26
	v_mov_b32_e32 v73, v26
	v_mov_b32_e32 v74, v26
	v_mov_b32_e32 v75, v26
	v_mov_b32_e32 v76, v26
	v_mov_b32_e32 v77, v26
	v_mov_b32_e32 v78, v26
	v_mov_b32_e32 v79, v26
.LBB3_21:
	s_or_b64 exec, exec, s[4:5]
	s_waitcnt vmcnt(5)
	v_cvt_f32_ubyte3_e32 v67, v23
	v_cvt_f32_ubyte2_e32 v66, v23
	v_cvt_f32_ubyte1_e32 v29, v22
	v_cvt_f32_ubyte0_e32 v28, v22
	v_cvt_f32_ubyte3_e32 v35, v22
	v_cvt_f32_ubyte2_e32 v34, v22
	v_cvt_f32_ubyte1_e32 v59, v23
	v_cvt_f32_ubyte0_e32 v58, v23
	v_fma_f32 v22, v66, v54, v72
	v_fma_f32 v23, v67, v54, v73
	v_cvt_f32_ubyte1_e32 v67, v24
	v_cvt_f32_ubyte0_e32 v66, v24
	v_fmac_f32_e32 v62, v66, v54
	v_fmac_f32_e32 v63, v67, v54
	v_cvt_f32_ubyte3_e32 v67, v24
	v_cvt_f32_ubyte2_e32 v66, v24
	v_fma_f32 v68, v66, v54, v64
	v_fma_f32 v69, v67, v54, v65
	v_cvt_f32_ubyte1_e32 v65, v25
	v_cvt_f32_ubyte0_e32 v64, v25
	v_fmac_f32_e32 v36, v64, v54
	v_fmac_f32_e32 v37, v65, v54
	v_cvt_f32_ubyte3_e32 v65, v25
	v_cvt_f32_ubyte2_e32 v64, v25
	v_fma_f32 v24, v64, v54, v26
	v_fma_f32 v25, v65, v54, v27
	v_and_b32_e32 v26, 0x80, v52
	v_fma_f32 v28, v28, v54, v78
	v_fma_f32 v29, v29, v54, v79
	v_fma_f32 v34, v34, v54, v76
	v_fma_f32 v35, v35, v54, v77
	v_fma_f32 v58, v58, v54, v74
	v_fma_f32 v59, v59, v54, v75
	v_cmp_ne_u32_e64 s[0:1], 0, v26
	s_and_saveexec_b64 s[4:5], s[0:1]
	s_cbranch_execz .LBB3_6
	v_and_b32_e32 v26, 63, v98
	v_mul_u32_u24_e32 v26, 0x220, v26
	v_or_b32_e32 v42, v49, v26
	ds_read2_b32 v[26:27], v42 offset1:8
	ds_read2_b32 v[52:53], v42 offset0:16 offset1:24
	ds_read2_b32 v[64:65], v42 offset0:32 offset1:40
	s_waitcnt lgkmcnt(2)
	v_add_f32_e32 v26, v28, v26
	v_add_f32_e32 v27, v29, v27
	s_waitcnt lgkmcnt(1)
	v_add_f32_e32 v28, v34, v52
	ds_write2_b32 v42, v26, v27 offset1:8
	v_add_f32_e32 v26, v35, v53
	ds_write2_b32 v42, v28, v26 offset0:16 offset1:24
	ds_read2_b32 v[26:27], v42 offset0:48 offset1:56
	s_waitcnt lgkmcnt(3)
	v_add_f32_e32 v28, v58, v64
	v_add_f32_e32 v29, v59, v65
	ds_write2_b32 v42, v28, v29 offset0:32 offset1:40
	ds_read2_b32 v[28:29], v42 offset0:64 offset1:72
	s_waitcnt lgkmcnt(2)
	v_add_f32_e32 v22, v22, v26
	v_add_f32_e32 v23, v23, v27
	ds_write2_b32 v42, v22, v23 offset0:48 offset1:56
	ds_read2_b32 v[22:23], v42 offset0:80 offset1:88
	s_waitcnt lgkmcnt(2)
	v_add_f32_e32 v26, v62, v28
	v_add_f32_e32 v27, v63, v29
	ds_write2_b32 v42, v26, v27 offset0:64 offset1:72
	ds_read2_b32 v[26:27], v42 offset0:96 offset1:104
	s_waitcnt lgkmcnt(2)
	v_add_f32_e32 v22, v68, v22
	v_add_f32_e32 v23, v69, v23
	ds_write2_b32 v42, v22, v23 offset0:80 offset1:88
	ds_read2_b32 v[22:23], v42 offset0:112 offset1:120
	ds_bpermute_b32 v28, v93, v95
	s_waitcnt lgkmcnt(3)
	v_add_f32_e32 v26, v36, v26
	v_add_f32_e32 v27, v37, v27
	ds_write2_b32 v42, v26, v27 offset0:96 offset1:104
	s_waitcnt lgkmcnt(2)
	v_add_f32_e32 v22, v24, v22
	v_add_f32_e32 v23, v25, v23
	v_mov_b32_e32 v24, 0
	ds_write2_b32 v42, v22, v23 offset0:112 offset1:120
	s_waitcnt lgkmcnt(2)
	v_lshrrev_b32_e32 v98, 16, v28
	v_mov_b32_e32 v25, v24
	v_mov_b32_e32 v36, v24
	v_mov_b32_e32 v37, v24
	v_mov_b32_e32 v68, v24
	v_mov_b32_e32 v69, v24
	v_mov_b32_e32 v62, v24
	v_mov_b32_e32 v63, v24
	v_mov_b32_e32 v22, v24
	v_mov_b32_e32 v23, v24
	v_mov_b32_e32 v58, v24
	v_mov_b32_e32 v59, v24
	v_mov_b32_e32 v34, v24
	v_mov_b32_e32 v35, v24
	v_mov_b32_e32 v28, v24
	v_mov_b32_e32 v29, v24
	s_branch .LBB3_6

.LBB3_26:
	s_or_b64 exec, exec, s[0:1]
	v_and_b32_e32 v62, 63, v0
	v_bfe_u32 v63, v0, 5, 1
	v_lshrrev_b32_e32 v64, 6, v0
	v_and_b32_e32 v65, 31, v0
	s_setprio 0
	s_waitcnt vmcnt(1)
	v_lshlrev_b32_e32 v10, 4, v62
	v_lshl_or_b32 v10, v64, 13, v10
	v_mov_b32_e32 v11, 0
	v_lshl_add_u64 v[12:13], s[12:13], 0, v[10:11]
	s_movk_i32 s0, 0x1000
	s_waitcnt lgkmcnt(0)
	global_load_dwordx4 v[6:9], v[38:39], off
	global_load_dwordx4 v[2:5], v[40:41], off
	global_load_dwordx4 v[16:19], v10, s[12:13]
	global_load_dwordx4 v[56:59], v10, s[12:13] offset:1024
	global_load_dwordx4 v[52:55], v10, s[12:13] offset:2048
	global_load_dwordx4 v[48:51], v10, s[12:13] offset:3072
	v_add_co_u32_e32 v10, vcc, s0, v12
	v_lshrrev_b32_e32 v23, 4, v0
	s_nop 0
	v_addc_co_u32_e32 v11, vcc, 0, v13, vcc
	global_load_dwordx4 v[44:47], v[10:11], off
	global_load_dwordx4 v[40:43], v[10:11], off offset:1024
	global_load_dwordx4 v[36:39], v[10:11], off offset:2048
	global_load_dwordx4 v[32:35], v[10:11], off offset:3072
	v_lshlrev_b32_e32 v10, 1, v0
	v_and_b32_e32 v11, 28, v10
	v_lshlrev_b32_e32 v10, 8, v0
	v_and_b32_e32 v21, 0x100, v10
	v_mul_u32_u24_e32 v10, 0x220, v23
	v_or_b32_e32 v10, v11, v10
	v_lshlrev_b32_e32 v0, 2, v23
	v_add_u32_e32 v26, v10, v21
	s_barrier
	ds_read_b32 v0, v0 offset:38912
	ds_read2_b32 v[12:13], v26 offset1:8
	ds_read2_b32 v[14:15], v26 offset0:16 offset1:24
	v_lshrrev_b32_e32 v66, 4, v84
	v_lshrrev_b32_e32 v67, 4, v83
	v_lshrrev_b32_e32 v68, 4, v82
	v_lshlrev_b32_e32 v10, 2, v66
	v_lshlrev_b32_e32 v22, 2, v67
	v_lshlrev_b32_e32 v24, 2, v68
	ds_read_b32 v20, v10 offset:38912
	ds_read_b32 v22, v22 offset:38912
	ds_read_b32 v10, v24 offset:38912
	ds_read2_b32 v[24:25], v26 offset0:32 offset1:40
	s_waitcnt lgkmcnt(5)
	v_fma_mixlo_f16 v69, v0, v12, 0
	v_mov_b32_e32 v12, v13
	s_waitcnt lgkmcnt(4)
	v_mov_b32_e32 v13, v14
	v_pk_mul_f32 v[12:13], v[0:1], v[12:13] op_sel_hi:[0,1]
	v_cvt_pk_f16_f32 v70, v12, v13
	v_mov_b32_e32 v12, v15
	s_waitcnt lgkmcnt(0)
	v_mov_b32_e32 v13, v24
	v_pk_mul_f32 v[12:13], v[0:1], v[12:13] op_sel_hi:[0,1]
	v_cvt_pk_f16_f32 v71, v12, v13
	v_mul_u32_u24_e32 v13, 0x220, v66
	ds_read2_b32 v[26:27], v26 offset0:48 offset1:56
	v_or_b32_e32 v13, v11, v13
	v_add_u32_e32 v28, v13, v21
	ds_read2_b32 v[14:15], v28 offset1:8
	v_mov_b32_e32 v12, v25
	s_waitcnt lgkmcnt(1)
	v_mov_b32_e32 v13, v26
	ds_read2_b32 v[24:25], v28 offset0:16 offset1:24
	v_pk_mul_f32 v[12:13], v[0:1], v[12:13] op_sel_hi:[0,1]
	v_cvt_pk_f16_f32 v26, v12, v13
	s_waitcnt lgkmcnt(1)
	v_fma_mixlo_f16 v72, v20, v14, 0
	v_mov_b32_e32 v12, v15
	ds_read2_b32 v[14:15], v28 offset0:32 offset1:40
	s_waitcnt lgkmcnt(1)
	v_mov_b32_e32 v13, v24
	v_pk_mul_f32 v[12:13], v[20:21], v[12:13] op_sel_hi:[0,1]
	v_cvt_pk_f16_f32 v73, v12, v13
	v_mov_b32_e32 v12, v25
	s_waitcnt lgkmcnt(0)
	v_mov_b32_e32 v13, v14
	v_pk_mul_f32 v[12:13], v[20:21], v[12:13] op_sel_hi:[0,1]
	v_cvt_pk_f16_f32 v74, v12, v13
	v_mul_u32_u24_e32 v13, 0x220, v67
	ds_read2_b32 v[24:25], v28 offset0:48 offset1:56
	v_or_b32_e32 v13, v11, v13
	v_add_u32_e32 v30, v13, v21
	v_mov_b32_e32 v12, v15
	ds_read2_b32 v[14:15], v30 offset1:8
	s_waitcnt lgkmcnt(1)
	v_mov_b32_e32 v13, v24
	ds_read2_b32 v[28:29], v30 offset0:16 offset1:24
	v_pk_mul_f32 v[12:13], v[20:21], v[12:13] op_sel_hi:[0,1]
	v_cvt_pk_f16_f32 v24, v12, v13
	s_waitcnt lgkmcnt(1)
	v_fma_mixlo_f16 v75, v22, v14, 0
	v_mov_b32_e32 v12, v15
	ds_read2_b32 v[14:15], v30 offset0:32 offset1:40
	s_waitcnt lgkmcnt(1)
	v_mov_b32_e32 v13, v28
	v_pk_mul_f32 v[12:13], v[22:23], v[12:13] op_sel_hi:[0,1]
	v_cvt_pk_f16_f32 v76, v12, v13
	v_mov_b32_e32 v12, v29
	s_waitcnt lgkmcnt(0)
	v_mov_b32_e32 v13, v14
	v_pk_mul_f32 v[12:13], v[22:23], v[12:13] op_sel_hi:[0,1]
	v_cvt_pk_f16_f32 v77, v12, v13
	v_mul_u32_u24_e32 v13, 0x220, v68
	ds_read2_b32 v[28:29], v30 offset0:48 offset1:56
	v_or_b32_e32 v11, v11, v13
	v_add_u32_e32 v11, v11, v21
	v_mov_b32_e32 v12, v15
	ds_read2_b32 v[14:15], v11 offset1:8
	ds_read2_b32 v[30:31], v11 offset0:16 offset1:24
	s_waitcnt lgkmcnt(2)
	v_mov_b32_e32 v13, v28
	v_pk_mul_f32 v[12:13], v[22:23], v[12:13] op_sel_hi:[0,1]
	v_cvt_pk_f16_f32 v21, v12, v13
	s_waitcnt lgkmcnt(1)
	v_fma_mixlo_f16 v28, v10, v14, 0
	v_mov_b32_e32 v12, v15
	s_waitcnt lgkmcnt(0)
	v_mov_b32_e32 v13, v30
	ds_read2_b32 v[14:15], v11 offset0:32 offset1:40
	v_pk_mul_f32 v[12:13], v[10:11], v[12:13] op_sel_hi:[0,1]
	v_cvt_pk_f16_f32 v78, v12, v13
	v_mov_b32_e32 v12, v31
	ds_read2_b32 v[30:31], v11 offset0:48 offset1:56
	s_waitcnt lgkmcnt(1)
	v_mov_b32_e32 v13, v14
	v_pk_mul_f32 v[12:13], v[10:11], v[12:13] op_sel_hi:[0,1]
	v_cvt_pk_f16_f32 v11, v12, v13
	v_mov_b32_e32 v12, v15
	s_waitcnt lgkmcnt(0)
	v_mov_b32_e32 v13, v30
	v_pk_mul_f32 v[12:13], v[10:11], v[12:13] op_sel_hi:[0,1]
	v_and_b32_e32 v79, 0xf0, v81
	v_lshrrev_b32_e32 v15, 16, v26
	s_movk_i32 s0, 0x110
	v_cvt_pk_f16_f32 v30, v12, v13
	v_pack_b32_f16 v12, v69, v70
	v_alignbit_b32 v13, v71, v70, 16
	v_alignbit_b32 v14, v26, v71, 16
	v_fma_mixhi_f16 v15, v0, v27, 0
	v_mad_u32_u24 v0, v23, s0, v79
	s_barrier
	ds_write_b128 v0, v[12:15]
	v_lshrrev_b32_e32 v15, 16, v24
	v_pack_b32_f16 v12, v72, v73
	v_alignbit_b32 v13, v74, v73, 16
	v_alignbit_b32 v14, v24, v74, 16
	v_fma_mixhi_f16 v15, v20, v25, 0
	v_mad_u32_u24 v0, v66, s0, v79
	ds_write_b128 v0, v[12:15]
	v_lshrrev_b32_e32 v15, 16, v21
	v_pack_b32_f16 v12, v75, v76
	v_alignbit_b32 v13, v77, v76, 16
	v_alignbit_b32 v14, v21, v77, 16
	v_fma_mixhi_f16 v15, v22, v29, 0
	v_mad_u32_u24 v0, v67, s0, v79
	ds_write_b128 v0, v[12:15]
	v_lshlrev_b32_e32 v0, 2, v80
	ds_read_b32 v0, v0 offset:38912
	v_lshrrev_b32_e32 v15, 16, v30
	v_fma_mixhi_f16 v15, v10, v31, 0
	v_lshlrev_b32_e32 v10, 2, v1
	ds_read_b32 v24, v10 offset:38912
	s_waitcnt lgkmcnt(1)
	v_div_scale_f32 v10, s[4:5], v0, v0, s18
	v_alignbit_b32 v13, v11, v78, 16
	v_alignbit_b32 v14, v30, v11, 16
	v_rcp_f32_e32 v11, v10
	v_pack_b32_f16 v12, v28, v78
	v_mad_u32_u24 v20, v68, s0, v79
	ds_write_b128 v20, v[12:15]
	v_fma_f32 v12, -v10, v11, 1.0
	v_fmac_f32_e32 v11, v12, v11
	v_div_scale_f32 v12, vcc, s18, v0, s18
	v_mul_f32_e32 v13, v12, v11
	v_fma_f32 v14, -v10, v13, v12
	v_fmac_f32_e32 v13, v14, v11
	v_fma_f32 v10, -v10, v13, v12
	v_div_fmas_f32 v10, v10, v11, v13
	v_div_fixup_f32 v0, v10, v0, s18
	s_waitcnt vmcnt(9)
	v_cvt_f32_ubyte1_e32 v13, v8
	v_cvt_f32_ubyte0_e32 v12, v8
	v_pk_mul_f32 v[12:13], v[0:1], v[12:13] op_sel_hi:[0,1]
	v_cvt_f32_ubyte1_e32 v11, v6
	v_cvt_f32_ubyte0_e32 v10, v6
	v_cvt_pk_f16_f32 v20, v12, v13
	v_cvt_f32_ubyte3_e32 v13, v6
	v_cvt_f32_ubyte2_e32 v12, v6
	v_pk_mul_f32 v[10:11], v[0:1], v[10:11] op_sel_hi:[0,1]
	v_pk_mul_f32 v[12:13], v[0:1], v[12:13] op_sel_hi:[0,1]
	v_cvt_pk_f16_f32 v10, v10, v11
	v_cvt_pk_f16_f32 v11, v12, v13
	v_cvt_f32_ubyte3_e32 v13, v8
	v_cvt_f32_ubyte2_e32 v12, v8
	v_cvt_f32_ubyte1_e32 v15, v9
	v_cvt_f32_ubyte0_e32 v14, v9
	v_pk_mul_f32 v[12:13], v[0:1], v[12:13] op_sel_hi:[0,1]
	v_pk_mul_f32 v[14:15], v[0:1], v[14:15] op_sel_hi:[0,1]
	v_cvt_pk_f16_f32 v21, v12, v13
	v_cvt_f32_ubyte1_e32 v13, v7
	v_cvt_f32_ubyte0_e32 v12, v7
	v_cvt_pk_f16_f32 v22, v14, v15
	v_cvt_f32_ubyte3_e32 v15, v7
	v_cvt_f32_ubyte2_e32 v14, v7
	v_pk_mul_f32 v[12:13], v[0:1], v[12:13] op_sel_hi:[0,1]
	v_pk_mul_f32 v[6:7], v[0:1], v[14:15] op_sel_hi:[0,1]
	v_cvt_pk_f16_f32 v12, v12, v13
	v_cvt_pk_f16_f32 v13, v6, v7
	v_cvt_f32_ubyte3_e32 v7, v9
	v_cvt_f32_ubyte2_e32 v6, v9
	v_pk_mul_f32 v[6:7], v[0:1], v[6:7] op_sel_hi:[0,1]
	s_waitcnt lgkmcnt(1)
	v_div_scale_f32 v0, s[4:5], v24, v24, s18
	v_cvt_pk_f16_f32 v23, v6, v7
	v_rcp_f32_e32 v6, v0
	v_lshlrev_b32_e32 v25, 1, v60
	v_mad_u32_u24 v7, v80, s0, v25
	ds_write_b128 v7, v[10:13] offset:17408
	ds_write_b128 v7, v[20:23] offset:17424
	v_fma_f32 v7, -v0, v6, 1.0
	v_fmac_f32_e32 v6, v7, v6
	v_div_scale_f32 v7, vcc, s18, v24, s18
	v_mul_f32_e32 v8, v7, v6
	v_fma_f32 v9, -v0, v8, v7
	v_fmac_f32_e32 v8, v9, v6
	v_fma_f32 v0, -v0, v8, v7
	v_div_fmas_f32 v0, v0, v6, v8
	v_div_fixup_f32 v0, v0, v24, s18
	s_waitcnt vmcnt(8)
	v_cvt_f32_ubyte1_e32 v9, v4
	v_cvt_f32_ubyte0_e32 v8, v4
	v_pk_mul_f32 v[8:9], v[0:1], v[8:9] op_sel_hi:[0,1]
	v_cvt_f32_ubyte1_e32 v7, v2
	v_cvt_f32_ubyte0_e32 v6, v2
	v_cvt_pk_f16_f32 v10, v8, v9
	v_cvt_f32_ubyte3_e32 v9, v2
	v_cvt_f32_ubyte2_e32 v8, v2
	v_pk_mul_f32 v[6:7], v[0:1], v[6:7] op_sel_hi:[0,1]
	v_pk_mul_f32 v[8:9], v[0:1], v[8:9] op_sel_hi:[0,1]
	v_cvt_pk_f16_f32 v6, v6, v7
	v_cvt_pk_f16_f32 v7, v8, v9
	v_cvt_f32_ubyte3_e32 v9, v4
	v_cvt_f32_ubyte2_e32 v8, v4
	v_pk_mul_f32 v[8:9], v[0:1], v[8:9] op_sel_hi:[0,1]
	v_cvt_pk_f16_f32 v11, v8, v9
	v_cvt_f32_ubyte1_e32 v9, v3
	v_cvt_f32_ubyte0_e32 v8, v3
	v_cvt_f32_ubyte3_e32 v15, v3
	v_cvt_f32_ubyte2_e32 v14, v3
	v_pk_mul_f32 v[8:9], v[0:1], v[8:9] op_sel_hi:[0,1]
	v_pk_mul_f32 v[2:3], v[0:1], v[14:15] op_sel_hi:[0,1]
	v_cvt_pk_f16_f32 v8, v8, v9
	v_cvt_f32_ubyte1_e32 v13, v5
	v_cvt_f32_ubyte0_e32 v12, v5
	v_cvt_pk_f16_f32 v9, v2, v3
	v_cvt_f32_ubyte3_e32 v3, v5
	v_cvt_f32_ubyte2_e32 v2, v5
	v_pk_mul_f32 v[12:13], v[0:1], v[12:13] op_sel_hi:[0,1]
	v_pk_mul_f32 v[2:3], v[0:1], v[2:3] op_sel_hi:[0,1]
	v_mad_u32_u24 v0, v1, s0, v25
	v_cvt_pk_f16_f32 v12, v12, v13
	v_cvt_pk_f16_f32 v13, v2, v3
	ds_write_b128 v0, v[6:9] offset:17408
	ds_write_b128 v0, v[10:13] offset:17424
	v_lshlrev_b32_e32 v0, 4, v63
	v_mad_u32_u24 v60, v65, s0, v0
	s_waitcnt lgkmcnt(0)
	s_barrier
	ds_read_b128 v[0:3], v60
	ds_read_b128 v[66:69], v60 offset:32
	s_waitcnt vmcnt(7) lgkmcnt(1)
	v_mfma_f32_32x32x16_f16 v[0:15], v[0:3], v[16:19], 0
	ds_read_b128 v[20:23], v60 offset:8704
	ds_read_b128 v[70:73], v60 offset:8736
	s_add_i32 s0, s3, 32
	s_mov_b32 s4, 0xc350
	s_waitcnt lgkmcnt(1)
	v_mfma_f32_32x32x16_f16 v[16:31], v[20:23], v[16:19], 0
	s_waitcnt vmcnt(6)
	v_mfma_f32_32x32x16_f16 v[0:15], v[66:69], v[56:59], v[0:15]
	s_waitcnt lgkmcnt(0)
	v_mfma_f32_32x32x16_f16 v[16:31], v[70:73], v[56:59], v[16:31]
	ds_read_b128 v[56:59], v60 offset:64
	ds_read_b128 v[66:69], v60 offset:96
	s_waitcnt vmcnt(5) lgkmcnt(1)
	v_mfma_f32_32x32x16_f16 v[0:15], v[56:59], v[52:55], v[0:15]
	ds_read_b128 v[56:59], v60 offset:8768
	ds_read_b128 v[70:73], v60 offset:8800
	s_waitcnt lgkmcnt(1)
	v_mfma_f32_32x32x16_f16 v[16:31], v[56:59], v[52:55], v[16:31]
	s_waitcnt vmcnt(4)
	v_mfma_f32_32x32x16_f16 v[0:15], v[66:69], v[48:51], v[0:15]
	s_waitcnt lgkmcnt(0)
	v_mfma_f32_32x32x16_f16 v[16:31], v[70:73], v[48:51], v[16:31]
	ds_read_b128 v[48:51], v60 offset:128
	ds_read_b128 v[52:55], v60 offset:160
	s_waitcnt vmcnt(3) lgkmcnt(1)
	v_mfma_f32_32x32x16_f16 v[0:15], v[48:51], v[44:47], v[0:15]
	ds_read_b128 v[48:51], v60 offset:8832
	ds_read_b128 v[56:59], v60 offset:8864
	s_waitcnt lgkmcnt(1)
	v_mfma_f32_32x32x16_f16 v[16:31], v[48:51], v[44:47], v[16:31]
	s_waitcnt vmcnt(2)
	v_mfma_f32_32x32x16_f16 v[0:15], v[52:55], v[40:43], v[0:15]
	s_waitcnt lgkmcnt(0)
	v_mfma_f32_32x32x16_f16 v[16:31], v[56:59], v[40:43], v[16:31]
	ds_read_b128 v[40:43], v60 offset:192
	ds_read_b128 v[44:47], v60 offset:224
	s_waitcnt vmcnt(1) lgkmcnt(1)
	v_mfma_f32_32x32x16_f16 v[0:15], v[40:43], v[36:39], v[0:15]
	ds_read_b128 v[40:43], v60 offset:8896
	ds_read_b128 v[48:51], v60 offset:8928
	s_waitcnt lgkmcnt(1)
	v_mfma_f32_32x32x16_f16 v[16:31], v[40:43], v[36:39], v[16:31]
	v_lshl_or_b32 v36, v64, 5, v65
	v_lshlrev_b32_e32 v37, 2, v36
	global_load_dword v37, v37, s[14:15]
	s_waitcnt vmcnt(1)
	v_mfma_f32_32x32x16_f16 v[0:15], v[44:47], v[32:35], v[0:15]
	v_bfrev_b32_e32 v45, 1
	s_waitcnt lgkmcnt(0)
	v_mfma_f32_32x32x16_f16 v[16:31], v[48:51], v[32:35], v[16:31]
	s_waitcnt vmcnt(0)
	s_add_i32 s5, s3, 49
	s_cmp_le_u32 s5, s4
	s_cbranch_scc1 .Lfast_sum_l2
	s_nop 7
	v_add_f32_e32 v1, v37, v1
	s_nop 1
	v_add_f32_e32 v26, v37, v0
	v_mul_u32_u24_e32 v0, 0x440, v63
	v_lshl_add_u32 v0, v36, 1, v0
	ds_read_u16 v27, v0 offset:17408
	ds_read_u16 v28, v0 offset:17680
	ds_read_u16 v29, v0 offset:17952
	ds_read_u16 v30, v0 offset:18224
	ds_read_u16 v31, v0 offset:19584
	ds_read_u16 v32, v0 offset:19856
	ds_read_u16 v33, v0 offset:20128
	ds_read_u16 v34, v0 offset:20400
	ds_read_u16 v35, v0 offset:26112
	ds_read_u16 v38, v0 offset:26384
	ds_read_u16 v39, v0 offset:26656
	ds_read_u16 v40, v0 offset:26928
	ds_read_u16 v41, v0 offset:28288
	ds_read_u16 v42, v0 offset:28560
	ds_read_u16 v43, v0 offset:28832
	ds_read_u16 v44, v0 offset:29104
	s_waitcnt lgkmcnt(14)
	v_cvt_f32_f16_e32 v27, v27
	s_waitcnt lgkmcnt(7)
	v_cvt_f32_f16_e32 v35, v35
	v_add_f32_e32 v16, v37, v16
	v_lshlrev_b32_e32 v25, 2, v63
	v_add_f32_e32 v26, v26, v27
	v_add_f32_e32 v16, v16, v35
	v_max_f32_e32 v26, 0, v26
	v_max_f32_e32 v27, 0, v16
	v_add_u32_e32 v16, s3, v25
	v_add_f32_e32 v26, 0, v26
	v_cmp_gt_i32_e32 vcc, s4, v16
	v_add_u32_e32 v35, s0, v25
	v_add_f32_e32 v17, v37, v17
	v_cndmask_b32_e32 v26, 0, v26, vcc
	v_cmp_gt_i32_e32 vcc, s4, v35
	s_waitcnt lgkmcnt(6)
	v_cvt_f32_f16_e32 v35, v38
	v_add_f32_e32 v2, v37, v2
	v_cndmask_b32_e32 v27, v45, v27, vcc
	v_add_f32_e32 v26, v26, v27
	v_cvt_f32_f16_e32 v27, v28
	v_or_b32_e32 v28, 1, v25
	v_add_f32_e32 v17, v17, v35
	v_max_f32_e32 v17, 0, v17
	v_add_f32_e32 v1, v1, v27
	v_max_f32_e32 v1, 0, v1
	v_add_u32_e32 v27, s3, v28
	v_add_f32_e32 v1, v26, v1
	v_cmp_gt_i32_e32 vcc, s4, v27
	s_waitcnt lgkmcnt(5)
	v_cvt_f32_f16_e32 v27, v39
	v_add_f32_e32 v3, v37, v3
	v_cndmask_b32_e32 v1, v26, v1, vcc
	v_add_u32_e32 v26, s0, v28
	v_add_f32_e32 v17, v17, v1
	v_cmp_gt_i32_e32 vcc, s4, v26
	v_or_b32_e32 v26, 2, v25
	v_add_f32_e32 v4, v37, v4
	v_cndmask_b32_e32 v1, v1, v17, vcc
	v_cvt_f32_f16_e32 v17, v29
	v_add_f32_e32 v8, v37, v8
	v_add_f32_e32 v2, v2, v17
	v_max_f32_e32 v2, 0, v2
	v_add_f32_e32 v17, v37, v18
	v_add_u32_e32 v18, s3, v26
	v_add_f32_e32 v2, v1, v2
	v_cmp_gt_i32_e32 vcc, s4, v18
	v_add_f32_e32 v17, v17, v27
	s_waitcnt lgkmcnt(4)
	v_cvt_f32_f16_e32 v18, v40
	v_cndmask_b32_e32 v1, v1, v2, vcc
	v_add_u32_e32 v2, s0, v26
	v_cmp_gt_i32_e32 vcc, s4, v2
	v_cvt_f32_f16_e32 v2, v30
	v_max_f32_e32 v17, 0, v17
	v_add_f32_e32 v17, v17, v1
	v_cndmask_b32_e32 v1, v1, v17, vcc
	v_or_b32_e32 v17, 3, v25
	v_add_f32_e32 v2, v3, v2
	v_add_f32_e32 v3, v37, v19
	v_max_f32_e32 v2, 0, v2
	v_add_f32_e32 v3, v3, v18
	v_add_u32_e32 v18, s3, v17
	v_add_f32_e32 v2, v1, v2
	v_cmp_gt_i32_e32 vcc, s4, v18
	v_max_f32_e32 v3, 0, v3
	v_or_b32_e32 v19, 16, v25
	v_cndmask_b32_e32 v1, v1, v2, vcc
	v_add_u32_e32 v2, s0, v17
	v_cmp_gt_i32_e32 vcc, s4, v2
	v_cvt_f32_f16_e32 v2, v31
	s_waitcnt lgkmcnt(3)
	v_cvt_f32_f16_e32 v17, v41
	v_add_f32_e32 v3, v3, v1
	v_cndmask_b32_e32 v1, v1, v3, vcc
	v_or_b32_e32 v3, 8, v25
	v_add_f32_e32 v2, v4, v2
	v_add_f32_e32 v4, v37, v20
	v_max_f32_e32 v2, 0, v2
	v_add_f32_e32 v4, v4, v17
	v_add_u32_e32 v17, s3, v3
	v_add_f32_e32 v2, v1, v2
	v_cmp_gt_i32_e32 vcc, s4, v17
	v_max_f32_e32 v4, 0, v4
	s_nop 0
	v_cndmask_b32_e32 v1, v1, v2, vcc
	v_add_u32_e32 v2, s0, v3
	v_cmp_gt_i32_e32 vcc, s4, v2
	v_cvt_f32_f16_e32 v2, v32
	v_add_f32_e32 v3, v4, v1
	v_add_f32_e32 v4, v37, v5
	s_waitcnt lgkmcnt(2)
	v_cvt_f32_f16_e32 v5, v42
	v_cndmask_b32_e32 v1, v1, v3, vcc
	v_or_b32_e32 v3, 9, v25
	v_add_f32_e32 v2, v4, v2
	v_add_f32_e32 v4, v37, v21
	v_max_f32_e32 v2, 0, v2
	v_add_f32_e32 v4, v4, v5
	v_add_u32_e32 v5, s3, v3
	v_add_f32_e32 v2, v1, v2
	v_cmp_gt_i32_e32 vcc, s4, v5
	s_waitcnt lgkmcnt(1)
	v_cvt_f32_f16_e32 v5, v43
	v_max_f32_e32 v4, 0, v4
	v_cndmask_b32_e32 v1, v1, v2, vcc
	v_add_u32_e32 v2, s0, v3
	v_cmp_gt_i32_e32 vcc, s4, v2
	v_cvt_f32_f16_e32 v2, v33
	v_add_f32_e32 v3, v4, v1
	v_add_f32_e32 v4, v37, v6
	v_cndmask_b32_e32 v1, v1, v3, vcc
	v_or_b32_e32 v3, 10, v25
	v_add_f32_e32 v2, v4, v2
	v_add_f32_e32 v4, v37, v22
	v_max_f32_e32 v2, 0, v2
	v_add_f32_e32 v4, v4, v5
	v_add_u32_e32 v5, s3, v3
	v_add_f32_e32 v2, v1, v2
	v_cmp_gt_i32_e32 vcc, s4, v5
	s_waitcnt lgkmcnt(0)
	v_cvt_f32_f16_e32 v5, v44
	v_max_f32_e32 v4, 0, v4
	v_cndmask_b32_e32 v1, v1, v2, vcc
	v_add_u32_e32 v2, s0, v3
	v_cmp_gt_i32_e32 vcc, s4, v2
	v_cvt_f32_f16_e32 v2, v34
	v_add_f32_e32 v3, v4, v1
	v_add_f32_e32 v4, v37, v7
	v_cndmask_b32_e32 v1, v1, v3, vcc
	v_or_b32_e32 v3, 11, v25
	v_add_f32_e32 v2, v4, v2
	v_add_f32_e32 v4, v37, v23
	v_max_f32_e32 v2, 0, v2
	v_add_f32_e32 v4, v4, v5
	v_add_u32_e32 v5, s3, v3
	v_add_f32_e32 v2, v1, v2
	v_cmp_gt_i32_e32 vcc, s4, v5
	v_max_f32_e32 v4, 0, v4
	s_nop 0
	v_cndmask_b32_e32 v1, v1, v2, vcc
	v_add_u32_e32 v2, s0, v3
	v_add_f32_e32 v3, v4, v1
	v_cmp_gt_i32_e32 vcc, s4, v2
	s_nop 1
	v_cndmask_b32_e32 v1, v1, v3, vcc
	ds_read_u16 v2, v0 offset:30464
	ds_read_u16 v3, v0 offset:21760
	ds_read_u16 v4, v0 offset:22032
	ds_read_u16 v5, v0 offset:22304
	ds_read_u16 v6, v0 offset:22576
	ds_read_u16 v7, v0 offset:23936
	ds_read_u16 v17, v0 offset:24208
	ds_read_u16 v18, v0 offset:24480
	ds_read_u16 v0, v0 offset:24752
	s_waitcnt lgkmcnt(7)
	v_cvt_f32_f16_e32 v3, v3
	v_cvt_f32_f16_e32 v2, v2
	v_add_f32_e32 v3, v8, v3
	v_add_f32_e32 v8, v37, v24
	v_max_f32_e32 v3, 0, v3
	v_add_f32_e32 v2, v8, v2
	v_add_u32_e32 v8, s3, v19
	v_add_f32_e32 v3, v1, v3
	v_cmp_gt_i32_e32 vcc, s4, v8
	v_max_f32_e32 v2, 0, v2
	s_waitcnt lgkmcnt(0)
	v_cvt_f32_f16_e32 v0, v0
	v_cndmask_b32_e32 v1, v1, v3, vcc
	v_add_u32_e32 v3, s0, v19
	v_cmp_gt_i32_e64 s[0:1], s4, v3
	v_cvt_f32_f16_e32 v3, v4
	v_cmp_gt_u32_e32 vcc, 32, v62
	v_add_f32_e32 v2, v2, v1
	s_and_b64 s[0:1], vcc, s[0:1]
	v_cndmask_b32_e64 v1, v1, v2, s[0:1]
	v_add_f32_e32 v2, v37, v9
	v_add_f32_e32 v2, v2, v3
	v_cvt_f32_f16_e32 v4, v5
	v_max_f32_e32 v2, 0, v2
	v_add_u32_e32 v3, 17, v16
	v_add_f32_e32 v2, v1, v2
	v_cmp_gt_i32_e64 s[0:1], s4, v3
	v_add_u32_e32 v3, 18, v16
	s_nop 0
	v_cndmask_b32_e64 v1, v1, v2, s[0:1]
	v_add_f32_e32 v2, v37, v10
	v_add_f32_e32 v2, v2, v4
	v_cvt_f32_f16_e32 v4, v6
	v_max_f32_e32 v2, 0, v2
	v_add_f32_e32 v2, v1, v2
	v_cmp_gt_i32_e64 s[0:1], s4, v3
	v_add_u32_e32 v3, 19, v16
	s_nop 0
	v_cndmask_b32_e64 v1, v1, v2, s[0:1]
	v_add_f32_e32 v2, v37, v11
	v_add_f32_e32 v2, v2, v4
	v_cvt_f32_f16_e32 v4, v7
	v_max_f32_e32 v2, 0, v2
	v_add_f32_e32 v2, v1, v2
	v_cmp_gt_i32_e64 s[0:1], s4, v3
	v_add_u32_e32 v3, 24, v16
	s_nop 0
	v_cndmask_b32_e64 v1, v1, v2, s[0:1]
	v_add_f32_e32 v2, v37, v12
	v_add_f32_e32 v2, v2, v4
	v_cvt_f32_f16_e32 v4, v17
	v_max_f32_e32 v2, 0, v2
	v_add_f32_e32 v2, v1, v2
	v_cmp_gt_i32_e64 s[0:1], s4, v3
	v_add_u32_e32 v3, 25, v16
	s_nop 0
	v_cndmask_b32_e64 v1, v1, v2, s[0:1]
	v_add_f32_e32 v2, v37, v13
	v_add_f32_e32 v2, v2, v4
	v_cvt_f32_f16_e32 v4, v18
	v_max_f32_e32 v2, 0, v2
	v_add_f32_e32 v2, v1, v2
	v_cmp_gt_i32_e64 s[0:1], s4, v3
	v_add_u32_e32 v3, 26, v16
	s_nop 0
	v_cndmask_b32_e64 v1, v1, v2, s[0:1]
	v_add_f32_e32 v2, v37, v14
	v_add_f32_e32 v2, v2, v4
	v_max_f32_e32 v2, 0, v2
	v_add_f32_e32 v2, v1, v2
	v_cmp_gt_i32_e64 s[0:1], s4, v3
	s_nop 1
	v_cndmask_b32_e64 v1, v1, v2, s[0:1]
	v_add_f32_e32 v2, v37, v15
	v_add_f32_e32 v0, v2, v0
	v_max_f32_e32 v0, 0, v0
	v_add_u32_e32 v2, 27, v16
	v_add_f32_e32 v0, v1, v0
	v_cmp_gt_i32_e64 s[0:1], s4, v2
	v_and_b32_e32 v2, 64, v61
	v_add_u32_e32 v2, 64, v2
	v_cndmask_b32_e64 v0, v1, v0, s[0:1]
.Ljoin_sum_l2:
	v_xor_b32_e32 v1, 32, v61
	v_cmp_lt_i32_e64 s[0:1], v1, v2
	s_nop 1
	v_cndmask_b32_e64 v1, v61, v1, s[0:1]
	v_lshlrev_b32_e32 v1, 2, v1
	ds_bpermute_b32 v1, v1, v0
	s_and_saveexec_b64 s[0:1], vcc
	s_cbranch_execz .LBB3_28
	s_lshl_b32 s0, s2, 7
	s_and_b32 s0, s0, 0x780
	v_or_b32_e32 v2, s0, v36
	v_lshlrev_b32_e32 v2, 2, v2
	s_waitcnt lgkmcnt(0)
	v_add_f32_e32 v0, v0, v1
	global_atomic_add_f32 v2, v0, s[6:7]

.Lfast_sum_l2:
	v_mul_u32_u24_e32 v38, 0x440, v63
	v_lshl_add_u32 v38, v36, 1, v38
	ds_read_u16 v39, v38 offset:17408
	ds_read_u16 v40, v38 offset:17680
	ds_read_u16 v41, v38 offset:17952
	ds_read_u16 v42, v38 offset:18224
	ds_read_u16 v43, v38 offset:19584
	ds_read_u16 v44, v38 offset:19856
	ds_read_u16 v45, v38 offset:20128
	ds_read_u16 v46, v38 offset:20400
	ds_read_u16 v47, v38 offset:21760
	ds_read_u16 v48, v38 offset:22032
	ds_read_u16 v49, v38 offset:22304
	ds_read_u16 v50, v38 offset:22576
	ds_read_u16 v51, v38 offset:23936
	v_cmp_gt_u32_e32 vcc, 32, v62
	v_pk_add_f32 v[0:1], v[0:1], v[36:37] op_sel:[0,1]
	v_pk_add_f32 v[2:3], v[2:3], v[36:37] op_sel:[0,1]
	v_pk_add_f32 v[4:5], v[4:5], v[36:37] op_sel:[0,1]
	v_pk_add_f32 v[6:7], v[6:7], v[36:37] op_sel:[0,1]
	v_pk_add_f32 v[8:9], v[8:9], v[36:37] op_sel:[0,1]
	v_pk_add_f32 v[10:11], v[10:11], v[36:37] op_sel:[0,1]
	v_pk_add_f32 v[12:13], v[12:13], v[36:37] op_sel:[0,1]
	v_pk_add_f32 v[14:15], v[14:15], v[36:37] op_sel:[0,1]
	v_pk_add_f32 v[16:17], v[16:17], v[36:37] op_sel:[0,1]
	v_pk_add_f32 v[18:19], v[18:19], v[36:37] op_sel:[0,1]
	v_pk_add_f32 v[20:21], v[20:21], v[36:37] op_sel:[0,1]
	v_pk_add_f32 v[22:23], v[22:23], v[36:37] op_sel:[0,1]
	v_add_f32_e32 v24, v37, v24
	v_mov_b32_e32 v35, 0
	s_waitcnt lgkmcnt(0)
	ds_read_u16 v52, v38 offset:24208
	ds_read_u16 v53, v38 offset:24480
	ds_read_u16 v54, v38 offset:24752
	ds_read_u16 v55, v38 offset:26112
	ds_read_u16 v56, v38 offset:26384
	ds_read_u16 v57, v38 offset:26656
	ds_read_u16 v58, v38 offset:26928
	ds_read_u16 v59, v38 offset:28288
	ds_read_u16 v60, v38 offset:28560
	ds_read_u16 v32, v38 offset:28832
	ds_read_u16 v33, v38 offset:29104
	ds_read_u16 v34, v38 offset:30464
	v_fma_mix_f32 v0, v39, 1.0, v0 op_sel_hi:[1,0,0]
	v_max_f32_e32 v0, 0, v0
	v_add_f32_e32 v35, v35, v0
	v_fma_mix_f32 v1, v40, 1.0, v1 op_sel_hi:[1,0,0]
	v_max_f32_e32 v1, 0, v1
	v_add_f32_e32 v35, v35, v1
	v_fma_mix_f32 v2, v41, 1.0, v2 op_sel_hi:[1,0,0]
	v_max_f32_e32 v2, 0, v2
	v_add_f32_e32 v35, v35, v2
	v_fma_mix_f32 v3, v42, 1.0, v3 op_sel_hi:[1,0,0]
	v_max_f32_e32 v3, 0, v3
	v_add_f32_e32 v35, v35, v3
	v_fma_mix_f32 v4, v43, 1.0, v4 op_sel_hi:[1,0,0]
	v_max_f32_e32 v4, 0, v4
	v_add_f32_e32 v35, v35, v4
	v_fma_mix_f32 v5, v44, 1.0, v5 op_sel_hi:[1,0,0]
	v_max_f32_e32 v5, 0, v5
	v_add_f32_e32 v35, v35, v5
	v_fma_mix_f32 v6, v45, 1.0, v6 op_sel_hi:[1,0,0]
	v_max_f32_e32 v6, 0, v6
	v_add_f32_e32 v35, v35, v6
	v_fma_mix_f32 v7, v46, 1.0, v7 op_sel_hi:[1,0,0]
	v_max_f32_e32 v7, 0, v7
	v_add_f32_e32 v35, v35, v7
	v_fma_mix_f32 v8, v47, 1.0, v8 op_sel_hi:[1,0,0]
	v_max_f32_e32 v8, 0, v8
	v_add_f32_e32 v35, v35, v8
	v_fma_mix_f32 v9, v48, 1.0, v9 op_sel_hi:[1,0,0]
	v_max_f32_e32 v9, 0, v9
	v_add_f32_e32 v35, v35, v9
	v_fma_mix_f32 v10, v49, 1.0, v10 op_sel_hi:[1,0,0]
	v_max_f32_e32 v10, 0, v10
	v_add_f32_e32 v35, v35, v10
	v_fma_mix_f32 v11, v50, 1.0, v11 op_sel_hi:[1,0,0]
	v_max_f32_e32 v11, 0, v11
	v_add_f32_e32 v35, v35, v11
	v_fma_mix_f32 v12, v51, 1.0, v12 op_sel_hi:[1,0,0]
	v_max_f32_e32 v12, 0, v12
	v_add_f32_e32 v35, v35, v12
	s_waitcnt lgkmcnt(0)
	v_fma_mix_f32 v13, v52, 1.0, v13 op_sel_hi:[1,0,0]
	v_max_f32_e32 v13, 0, v13
	v_add_f32_e32 v35, v35, v13
	v_fma_mix_f32 v14, v53, 1.0, v14 op_sel_hi:[1,0,0]
	v_max_f32_e32 v14, 0, v14
	v_add_f32_e32 v35, v35, v14
	v_fma_mix_f32 v15, v54, 1.0, v15 op_sel_hi:[1,0,0]
	v_max_f32_e32 v15, 0, v15
	v_add_f32_e32 v35, v35, v15
	v_fma_mix_f32 v16, v55, 1.0, v16 op_sel_hi:[1,0,0]
	v_max_f32_e32 v16, 0, v16
	v_add_f32_e32 v35, v35, v16
	v_fma_mix_f32 v17, v56, 1.0, v17 op_sel_hi:[1,0,0]
	v_max_f32_e32 v17, 0, v17
	v_add_f32_e32 v35, v35, v17
	v_fma_mix_f32 v18, v57, 1.0, v18 op_sel_hi:[1,0,0]
	v_max_f32_e32 v18, 0, v18
	v_add_f32_e32 v35, v35, v18
	v_fma_mix_f32 v19, v58, 1.0, v19 op_sel_hi:[1,0,0]
	v_max_f32_e32 v19, 0, v19
	v_add_f32_e32 v35, v35, v19
	v_fma_mix_f32 v20, v59, 1.0, v20 op_sel_hi:[1,0,0]
	v_max_f32_e32 v20, 0, v20
	v_add_f32_e32 v35, v35, v20
	v_fma_mix_f32 v21, v60, 1.0, v21 op_sel_hi:[1,0,0]
	v_max_f32_e32 v21, 0, v21
	v_add_f32_e32 v35, v35, v21
	v_fma_mix_f32 v22, v32, 1.0, v22 op_sel_hi:[1,0,0]
	v_max_f32_e32 v22, 0, v22
	v_add_f32_e32 v35, v35, v22
	v_fma_mix_f32 v23, v33, 1.0, v23 op_sel_hi:[1,0,0]
	v_max_f32_e32 v23, 0, v23
	v_add_f32_e32 v35, v35, v23
	v_fma_mix_f32 v24, v34, 1.0, v24 op_sel_hi:[1,0,0]
	v_max_f32_e32 v24, 0, v24
	v_cndmask_b32_e32 v24, 0, v24, vcc
	v_add_f32_e32 v35, v35, v24
	v_and_b32_e32 v2, 64, v61
	v_add_u32_e32 v2, 64, v2
	v_mov_b32_e32 v0, v35
	s_branch .Ljoin_sum_l2
